# plus non-temporal loads for the one-shot ada_w stream in the modulation phase
# baseline (speedup 1.0000x reference)
.LBB0_132:
	v_lshl_add_u64 v[96:97], v[94:95], 0, s[8:9]
	v_add_co_u32_e32 v104, vcc, s10, v96
	ds_read_b128 v[20:23], v98
	ds_read_b128 v[16:19], v98 offset:16
	ds_read_b128 v[24:27], v98 offset:8192
	ds_read_b128 v[32:35], v98 offset:8208
	ds_read_b128 v[48:51], v98 offset:16384
	ds_read_b128 v[36:39], v98 offset:16400
	ds_read_b128 v[52:55], v98 offset:24576
	ds_read_b128 v[44:47], v98 offset:24592
	ds_read_b128 v[40:43], v98 offset:32
	ds_read_b128 v[28:31], v98 offset:48
	ds_read_b128 v[56:59], v98 offset:8224
	ds_read_b128 v[60:63], v98 offset:8240
	ds_read_b128 v[72:75], v98 offset:16416
	ds_read_b128 v[64:67], v98 offset:16432
	ds_read_b128 v[76:79], v98 offset:24608
	ds_read_b128 v[68:71], v98 offset:24624
	v_addc_co_u32_e32 v105, vcc, 0, v97, vcc
	v_add_co_u32_e32 v108, vcc, s11, v96
	global_load_dwordx4 v[100:103], v[96:97], off nt
	s_nop 0
	v_addc_co_u32_e32 v109, vcc, 0, v97, vcc
	v_add_co_u32_e32 v112, vcc, s16, v96
	s_waitcnt lgkmcnt(14)
	v_mov_b32_e32 v82, v23
	v_addc_co_u32_e32 v113, vcc, 0, v97, vcc
	v_add_co_u32_e32 v116, vcc, s17, v96
	s_waitcnt lgkmcnt(11)
	v_mov_b32_e32 v164, v51
	v_addc_co_u32_e32 v117, vcc, 0, v97, vcc
	v_add_co_u32_e32 v120, vcc, s18, v96
	s_waitcnt lgkmcnt(9)
	v_mov_b32_e32 v166, v55
	v_addc_co_u32_e32 v121, vcc, 0, v97, vcc
	v_add_co_u32_e32 v124, vcc, s19, v96
	v_mov_b32_e32 v168, v19
	s_nop 0
	v_addc_co_u32_e32 v125, vcc, 0, v97, vcc
	v_add_co_u32_e32 v128, vcc, s20, v96
	v_mov_b32_e32 v170, v35
	s_nop 0
	v_addc_co_u32_e32 v129, vcc, 0, v97, vcc
	v_add_co_u32_e32 v132, vcc, s21, v96
	v_mov_b32_e32 v172, v39
	s_nop 0
	v_addc_co_u32_e32 v133, vcc, 0, v97, vcc
	v_add_co_u32_e32 v136, vcc, s22, v96
	s_waitcnt lgkmcnt(8)
	v_mov_b32_e32 v174, v47
	v_addc_co_u32_e32 v137, vcc, 0, v97, vcc
	v_add_co_u32_e32 v140, vcc, s23, v96
	s_waitcnt lgkmcnt(7)
	v_mov_b32_e32 v176, v43
	v_addc_co_u32_e32 v141, vcc, 0, v97, vcc
	v_add_co_u32_e32 v144, vcc, s24, v96
	s_waitcnt lgkmcnt(5)
	v_mov_b32_e32 v178, v59
	v_addc_co_u32_e32 v145, vcc, 0, v97, vcc
	v_add_co_u32_e32 v148, vcc, s25, v96
	s_waitcnt lgkmcnt(3)
	v_mov_b32_e32 v180, v75
	v_addc_co_u32_e32 v149, vcc, 0, v97, vcc
	v_add_co_u32_e32 v152, vcc, s26, v96
	s_waitcnt lgkmcnt(1)
	v_mov_b32_e32 v182, v79
	v_addc_co_u32_e32 v153, vcc, 0, v97, vcc
	v_add_co_u32_e32 v156, vcc, s27, v96
	s_add_u32 s8, s8, 0xc0000
	s_nop 0
	v_addc_co_u32_e32 v157, vcc, 0, v97, vcc
	v_add_co_u32_e32 v96, vcc, s28, v96
	s_addc_u32 s9, s9, 0
	s_nop 0
	v_addc_co_u32_e32 v97, vcc, 0, v97, vcc
	global_load_dwordx4 v[104:107], v[104:105], off nt
	s_nop 0
	global_load_dwordx4 v[108:111], v[108:109], off nt
	s_nop 0
	global_load_dwordx4 v[112:115], v[112:113], off nt
	s_nop 0
	global_load_dwordx4 v[116:119], v[116:117], off nt
	s_nop 0
	global_load_dwordx4 v[120:123], v[120:121], off nt
	s_nop 0
	global_load_dwordx4 v[124:127], v[124:125], off nt
	s_nop 0
	global_load_dwordx4 v[128:131], v[128:129], off nt
	s_nop 0
	global_load_dwordx4 v[132:135], v[132:133], off nt
	s_nop 0
	global_load_dwordx4 v[136:139], v[136:137], off nt
	s_nop 0
	global_load_dwordx4 v[140:143], v[140:141], off nt
	s_nop 0
	global_load_dwordx4 v[144:147], v[144:145], off nt
	s_nop 0
	global_load_dwordx4 v[148:151], v[148:149], off nt
	s_nop 0
	global_load_dwordx4 v[152:155], v[152:153], off nt
	s_nop 0
	global_load_dwordx4 v[156:159], v[156:157], off nt
	s_nop 0
	global_load_dwordx4 v[160:163], v[96:97], off nt
	v_mov_b32_e32 v96, v27
	v_mov_b32_e32 v184, v31
	v_mov_b32_e32 v186, v63
	v_mov_b32_e32 v188, v67
	s_waitcnt lgkmcnt(0)
	v_mov_b32_e32 v190, v71
	v_add_u32_e32 v98, 64, v98
	s_cmp_eq_u32 s8, 0x300000
	s_waitcnt vmcnt(15)
	v_pk_fma_f32 v[14:15], v[102:103], v[20:21], v[14:15] op_sel_hi:[1,0,1]
	v_pk_fma_f32 v[12:13], v[100:101], v[20:21], v[12:13] op_sel_hi:[1,0,1]
	v_pk_fma_f32 v[10:11], v[102:103], v[24:25], v[10:11] op_sel_hi:[1,0,1]
	v_pk_fma_f32 v[8:9], v[100:101], v[24:25], v[8:9] op_sel_hi:[1,0,1]
	v_pk_fma_f32 v[6:7], v[102:103], v[48:49], v[6:7] op_sel_hi:[1,0,1]
	v_pk_fma_f32 v[4:5], v[100:101], v[48:49], v[4:5] op_sel_hi:[1,0,1]
	v_pk_fma_f32 v[2:3], v[102:103], v[52:53], v[2:3] op_sel_hi:[1,0,1]
	v_pk_fma_f32 v[0:1], v[100:101], v[52:53], v[0:1] op_sel_hi:[1,0,1]
	s_waitcnt vmcnt(14)
	v_pk_fma_f32 v[12:13], v[104:105], v[20:21], v[12:13] op_sel:[0,1,0]
	v_pk_fma_f32 v[14:15], v[106:107], v[20:21], v[14:15] op_sel:[0,1,0]
	v_pk_fma_f32 v[8:9], v[104:105], v[24:25], v[8:9] op_sel:[0,1,0]
	v_pk_fma_f32 v[10:11], v[106:107], v[24:25], v[10:11] op_sel:[0,1,0]
	v_pk_fma_f32 v[4:5], v[104:105], v[48:49], v[4:5] op_sel:[0,1,0]
	v_pk_fma_f32 v[6:7], v[106:107], v[48:49], v[6:7] op_sel:[0,1,0]
	v_pk_fma_f32 v[0:1], v[104:105], v[52:53], v[0:1] op_sel:[0,1,0]
	v_pk_fma_f32 v[2:3], v[106:107], v[52:53], v[2:3] op_sel:[0,1,0]
	s_waitcnt vmcnt(13)
	v_pk_fma_f32 v[14:15], v[110:111], v[22:23], v[14:15] op_sel_hi:[1,0,1]
	v_pk_fma_f32 v[12:13], v[108:109], v[22:23], v[12:13] op_sel_hi:[1,0,1]
	v_pk_fma_f32 v[10:11], v[110:111], v[26:27], v[10:11] op_sel_hi:[1,0,1]
	v_pk_fma_f32 v[8:9], v[108:109], v[26:27], v[8:9] op_sel_hi:[1,0,1]
	v_pk_fma_f32 v[6:7], v[110:111], v[50:51], v[6:7] op_sel_hi:[1,0,1]
	v_pk_fma_f32 v[4:5], v[108:109], v[50:51], v[4:5] op_sel_hi:[1,0,1]
	v_pk_fma_f32 v[2:3], v[110:111], v[54:55], v[2:3] op_sel_hi:[1,0,1]
	v_pk_fma_f32 v[0:1], v[108:109], v[54:55], v[0:1] op_sel_hi:[1,0,1]
	s_waitcnt vmcnt(12)
	v_pk_fma_f32 v[14:15], v[114:115], v[82:83], v[14:15] op_sel_hi:[1,0,1]
	v_pk_fma_f32 v[12:13], v[112:113], v[82:83], v[12:13] op_sel_hi:[1,0,1]
	v_pk_fma_f32 v[10:11], v[114:115], v[96:97], v[10:11] op_sel_hi:[1,0,1]
	v_pk_fma_f32 v[8:9], v[112:113], v[96:97], v[8:9] op_sel_hi:[1,0,1]
	v_pk_fma_f32 v[6:7], v[114:115], v[164:165], v[6:7] op_sel_hi:[1,0,1]
	v_pk_fma_f32 v[4:5], v[112:113], v[164:165], v[4:5] op_sel_hi:[1,0,1]
	v_pk_fma_f32 v[2:3], v[114:115], v[166:167], v[2:3] op_sel_hi:[1,0,1]
	v_pk_fma_f32 v[0:1], v[112:113], v[166:167], v[0:1] op_sel_hi:[1,0,1]
	s_waitcnt vmcnt(11)
	v_pk_fma_f32 v[14:15], v[118:119], v[16:17], v[14:15] op_sel_hi:[1,0,1]
	v_pk_fma_f32 v[12:13], v[116:117], v[16:17], v[12:13] op_sel_hi:[1,0,1]
	v_pk_fma_f32 v[10:11], v[118:119], v[32:33], v[10:11] op_sel_hi:[1,0,1]
	v_pk_fma_f32 v[8:9], v[116:117], v[32:33], v[8:9] op_sel_hi:[1,0,1]
	v_pk_fma_f32 v[6:7], v[118:119], v[36:37], v[6:7] op_sel_hi:[1,0,1]
	v_pk_fma_f32 v[4:5], v[116:117], v[36:37], v[4:5] op_sel_hi:[1,0,1]
	v_pk_fma_f32 v[2:3], v[118:119], v[44:45], v[2:3] op_sel_hi:[1,0,1]
	v_pk_fma_f32 v[0:1], v[116:117], v[44:45], v[0:1] op_sel_hi:[1,0,1]
	s_waitcnt vmcnt(10)
	v_pk_fma_f32 v[14:15], v[122:123], v[16:17], v[14:15] op_sel:[0,1,0]
	v_pk_fma_f32 v[12:13], v[120:121], v[16:17], v[12:13] op_sel:[0,1,0]
	v_pk_fma_f32 v[10:11], v[122:123], v[32:33], v[10:11] op_sel:[0,1,0]
	v_pk_fma_f32 v[8:9], v[120:121], v[32:33], v[8:9] op_sel:[0,1,0]
	v_pk_fma_f32 v[6:7], v[122:123], v[36:37], v[6:7] op_sel:[0,1,0]
	v_pk_fma_f32 v[4:5], v[120:121], v[36:37], v[4:5] op_sel:[0,1,0]
	v_pk_fma_f32 v[2:3], v[122:123], v[44:45], v[2:3] op_sel:[0,1,0]
	v_pk_fma_f32 v[0:1], v[120:121], v[44:45], v[0:1] op_sel:[0,1,0]
	s_waitcnt vmcnt(9)
	v_pk_fma_f32 v[14:15], v[126:127], v[18:19], v[14:15] op_sel_hi:[1,0,1]
	v_pk_fma_f32 v[12:13], v[124:125], v[18:19], v[12:13] op_sel_hi:[1,0,1]
	v_pk_fma_f32 v[10:11], v[126:127], v[34:35], v[10:11] op_sel_hi:[1,0,1]
	v_pk_fma_f32 v[8:9], v[124:125], v[34:35], v[8:9] op_sel_hi:[1,0,1]
	v_pk_fma_f32 v[6:7], v[126:127], v[38:39], v[6:7] op_sel_hi:[1,0,1]
	v_pk_fma_f32 v[4:5], v[124:125], v[38:39], v[4:5] op_sel_hi:[1,0,1]
	v_pk_fma_f32 v[2:3], v[126:127], v[46:47], v[2:3] op_sel_hi:[1,0,1]
	v_pk_fma_f32 v[0:1], v[124:125], v[46:47], v[0:1] op_sel_hi:[1,0,1]
	s_waitcnt vmcnt(8)
	v_pk_fma_f32 v[14:15], v[130:131], v[168:169], v[14:15] op_sel_hi:[1,0,1]
	v_pk_fma_f32 v[12:13], v[128:129], v[168:169], v[12:13] op_sel_hi:[1,0,1]
	v_pk_fma_f32 v[10:11], v[130:131], v[170:171], v[10:11] op_sel_hi:[1,0,1]
	v_pk_fma_f32 v[8:9], v[128:129], v[170:171], v[8:9] op_sel_hi:[1,0,1]
	v_pk_fma_f32 v[6:7], v[130:131], v[172:173], v[6:7] op_sel_hi:[1,0,1]
	v_pk_fma_f32 v[4:5], v[128:129], v[172:173], v[4:5] op_sel_hi:[1,0,1]
	v_pk_fma_f32 v[2:3], v[130:131], v[174:175], v[2:3] op_sel_hi:[1,0,1]
	v_pk_fma_f32 v[0:1], v[128:129], v[174:175], v[0:1] op_sel_hi:[1,0,1]
	s_waitcnt vmcnt(7)
	v_pk_fma_f32 v[14:15], v[134:135], v[40:41], v[14:15] op_sel_hi:[1,0,1]
	v_pk_fma_f32 v[12:13], v[132:133], v[40:41], v[12:13] op_sel_hi:[1,0,1]
	v_pk_fma_f32 v[10:11], v[134:135], v[56:57], v[10:11] op_sel_hi:[1,0,1]
	v_pk_fma_f32 v[8:9], v[132:133], v[56:57], v[8:9] op_sel_hi:[1,0,1]
	v_pk_fma_f32 v[6:7], v[134:135], v[72:73], v[6:7] op_sel_hi:[1,0,1]
	v_pk_fma_f32 v[4:5], v[132:133], v[72:73], v[4:5] op_sel_hi:[1,0,1]
	v_pk_fma_f32 v[2:3], v[134:135], v[76:77], v[2:3] op_sel_hi:[1,0,1]
	v_pk_fma_f32 v[0:1], v[132:133], v[76:77], v[0:1] op_sel_hi:[1,0,1]
	s_waitcnt vmcnt(6)
	v_pk_fma_f32 v[14:15], v[138:139], v[40:41], v[14:15] op_sel:[0,1,0]
	v_pk_fma_f32 v[12:13], v[136:137], v[40:41], v[12:13] op_sel:[0,1,0]
	v_pk_fma_f32 v[10:11], v[138:139], v[56:57], v[10:11] op_sel:[0,1,0]
	v_pk_fma_f32 v[8:9], v[136:137], v[56:57], v[8:9] op_sel:[0,1,0]
	v_pk_fma_f32 v[6:7], v[138:139], v[72:73], v[6:7] op_sel:[0,1,0]
	v_pk_fma_f32 v[4:5], v[136:137], v[72:73], v[4:5] op_sel:[0,1,0]
	v_pk_fma_f32 v[2:3], v[138:139], v[76:77], v[2:3] op_sel:[0,1,0]
	v_pk_fma_f32 v[0:1], v[136:137], v[76:77], v[0:1] op_sel:[0,1,0]
	s_waitcnt vmcnt(5)
	v_pk_fma_f32 v[14:15], v[142:143], v[42:43], v[14:15] op_sel_hi:[1,0,1]
	v_pk_fma_f32 v[12:13], v[140:141], v[42:43], v[12:13] op_sel_hi:[1,0,1]
	v_pk_fma_f32 v[10:11], v[142:143], v[58:59], v[10:11] op_sel_hi:[1,0,1]
	v_pk_fma_f32 v[8:9], v[140:141], v[58:59], v[8:9] op_sel_hi:[1,0,1]
	v_pk_fma_f32 v[6:7], v[142:143], v[74:75], v[6:7] op_sel_hi:[1,0,1]
	v_pk_fma_f32 v[4:5], v[140:141], v[74:75], v[4:5] op_sel_hi:[1,0,1]
	v_pk_fma_f32 v[2:3], v[142:143], v[78:79], v[2:3] op_sel_hi:[1,0,1]
	v_pk_fma_f32 v[0:1], v[140:141], v[78:79], v[0:1] op_sel_hi:[1,0,1]
	s_waitcnt vmcnt(4)
	v_pk_fma_f32 v[14:15], v[146:147], v[176:177], v[14:15] op_sel_hi:[1,0,1]
	v_pk_fma_f32 v[12:13], v[144:145], v[176:177], v[12:13] op_sel_hi:[1,0,1]
	v_pk_fma_f32 v[10:11], v[146:147], v[178:179], v[10:11] op_sel_hi:[1,0,1]
	v_pk_fma_f32 v[8:9], v[144:145], v[178:179], v[8:9] op_sel_hi:[1,0,1]
	v_pk_fma_f32 v[6:7], v[146:147], v[180:181], v[6:7] op_sel_hi:[1,0,1]
	v_pk_fma_f32 v[4:5], v[144:145], v[180:181], v[4:5] op_sel_hi:[1,0,1]
	v_pk_fma_f32 v[2:3], v[146:147], v[182:183], v[2:3] op_sel_hi:[1,0,1]
	v_pk_fma_f32 v[0:1], v[144:145], v[182:183], v[0:1] op_sel_hi:[1,0,1]
	s_waitcnt vmcnt(3)
	v_pk_fma_f32 v[14:15], v[150:151], v[28:29], v[14:15] op_sel_hi:[1,0,1]
	v_pk_fma_f32 v[12:13], v[148:149], v[28:29], v[12:13] op_sel_hi:[1,0,1]
	v_pk_fma_f32 v[10:11], v[150:151], v[60:61], v[10:11] op_sel_hi:[1,0,1]
	v_pk_fma_f32 v[8:9], v[148:149], v[60:61], v[8:9] op_sel_hi:[1,0,1]
	v_pk_fma_f32 v[6:7], v[150:151], v[64:65], v[6:7] op_sel_hi:[1,0,1]
	v_pk_fma_f32 v[4:5], v[148:149], v[64:65], v[4:5] op_sel_hi:[1,0,1]
	v_pk_fma_f32 v[2:3], v[150:151], v[68:69], v[2:3] op_sel_hi:[1,0,1]
	v_pk_fma_f32 v[0:1], v[148:149], v[68:69], v[0:1] op_sel_hi:[1,0,1]
	s_waitcnt vmcnt(2)
	v_pk_fma_f32 v[14:15], v[154:155], v[28:29], v[14:15] op_sel:[0,1,0]
	v_pk_fma_f32 v[12:13], v[152:153], v[28:29], v[12:13] op_sel:[0,1,0]
	v_pk_fma_f32 v[10:11], v[154:155], v[60:61], v[10:11] op_sel:[0,1,0]
	v_pk_fma_f32 v[8:9], v[152:153], v[60:61], v[8:9] op_sel:[0,1,0]
	v_pk_fma_f32 v[6:7], v[154:155], v[64:65], v[6:7] op_sel:[0,1,0]
	v_pk_fma_f32 v[4:5], v[152:153], v[64:65], v[4:5] op_sel:[0,1,0]
	v_pk_fma_f32 v[2:3], v[154:155], v[68:69], v[2:3] op_sel:[0,1,0]
	v_pk_fma_f32 v[0:1], v[152:153], v[68:69], v[0:1] op_sel:[0,1,0]
	s_waitcnt vmcnt(1)
	v_pk_fma_f32 v[14:15], v[158:159], v[30:31], v[14:15] op_sel_hi:[1,0,1]
	v_pk_fma_f32 v[12:13], v[156:157], v[30:31], v[12:13] op_sel_hi:[1,0,1]
	v_pk_fma_f32 v[10:11], v[158:159], v[62:63], v[10:11] op_sel_hi:[1,0,1]
	v_pk_fma_f32 v[8:9], v[156:157], v[62:63], v[8:9] op_sel_hi:[1,0,1]
	v_pk_fma_f32 v[6:7], v[158:159], v[66:67], v[6:7] op_sel_hi:[1,0,1]
	v_pk_fma_f32 v[4:5], v[156:157], v[66:67], v[4:5] op_sel_hi:[1,0,1]
	v_pk_fma_f32 v[2:3], v[158:159], v[70:71], v[2:3] op_sel_hi:[1,0,1]
	v_pk_fma_f32 v[0:1], v[156:157], v[70:71], v[0:1] op_sel_hi:[1,0,1]
	s_waitcnt vmcnt(0)
	v_pk_fma_f32 v[14:15], v[162:163], v[184:185], v[14:15] op_sel_hi:[1,0,1]
	v_pk_fma_f32 v[12:13], v[160:161], v[184:185], v[12:13] op_sel_hi:[1,0,1]
	v_pk_fma_f32 v[10:11], v[162:163], v[186:187], v[10:11] op_sel_hi:[1,0,1]
	v_pk_fma_f32 v[8:9], v[160:161], v[186:187], v[8:9] op_sel_hi:[1,0,1]
	v_pk_fma_f32 v[6:7], v[162:163], v[188:189], v[6:7] op_sel_hi:[1,0,1]
	v_pk_fma_f32 v[4:5], v[160:161], v[188:189], v[4:5] op_sel_hi:[1,0,1]
	v_pk_fma_f32 v[2:3], v[162:163], v[190:191], v[2:3] op_sel_hi:[1,0,1]
	v_pk_fma_f32 v[0:1], v[160:161], v[190:191], v[0:1] op_sel_hi:[1,0,1]
	s_cbranch_scc0 .LBB0_132
	v_lshlrev_b32_e32 v16, 2, v87
	v_lshl_or_b32 v18, v90, 7, v16
	v_mov_b64_e32 v[16:17], s[4:5]
	v_mad_i64_i32 v[16:17], s[8:9], v18, s10, v[16:17]
	v_lshl_add_u64 v[16:17], v[92:93], 2, v[16:17]
	v_mov_b32_e32 v87, v83
	v_lshl_add_u64 v[16:17], v[16:17], 0, v[86:87]
	global_store_dwordx4 v[16:17], v[12:15], off
	v_add_u32_e32 v81, s1, v81
	v_add_u16_e32 v91, s1, v91
	v_add_co_u32_e32 v12, vcc, 0xc000, v16
	s_nop 1
	v_addc_co_u32_e32 v13, vcc, 0, v17, vcc
	global_store_dwordx4 v[12:13], v[8:11], off
	s_nop 1
	v_add_co_u32_e32 v8, vcc, 0x18000, v16
	s_nop 1
	v_addc_co_u32_e32 v9, vcc, 0, v17, vcc
	global_store_dwordx4 v[8:9], v[4:7], off
	s_nop 1
	v_add_co_u32_e32 v4, vcc, 0x24000, v16
	s_nop 1
	v_addc_co_u32_e32 v5, vcc, 0, v17, vcc
	v_cmp_lt_i32_e32 vcc, s29, v81
	s_or_b64 s[6:7], vcc, s[6:7]
	global_store_dwordx4 v[4:5], v[0:3], off
	s_andn2_b64 exec, exec, s[6:7]
	s_cbranch_execnz .LBB0_131
